# v36: SGU unit MFMA section: LDS reads of k-step k+1 batched ahead of k-step k's MFMAs with counted lgkmcnt (was one lgkmcnt(0) per read pair)
# baseline (speedup 1.0000x reference)
; #define GAS __attribute__((address_space(1)))
; #define LAS __attribute__((address_space(3)))
; __device__ __forceinline__ unsigned pk2(float lo, float hi) { return pg8::cvt_pk_bf16(lo, hi); }
; __device__ __forceinline__ void sgu_unit(Frame& F, int unit) {
;     const int ck = unit >> 3, g = unit & 7, r0 = ck * GMC, c0 = g * GMGW, tid = F.tid, lane = F.lane, w = F.wave, hi = lane >> 5, l31 = lane & 31;
;     LAS unsigned char* L = F.lds;
;     const int rs_ = tid >> 5, q_ = tid & 31;
;     __syncthreads();
; #pragma unroll
;     for (int i = 0; i < 8; ++i) *(LAS v4u*)(L + (rs_ + 16 * i) * 512 + q_ * 16) = *(const GAS v4u*)(F.PROJ + (size_t)(r0 + rs_ + 16 * i) * PNP + PGV + c0 + 8 * q_);
;     { const f32x4 q = *(const GAS f32x4*)(F.RS + r0 + 4 * q_);
; #pragma unroll
;       for (int i = 0; i < 8; ++i) { const int t_ = rs_ + 16 * i; const f32x4 wv = *(const GAS f32x4*)(F.sgw + ((size_t)(g * GMC + t_)) * GMC + 4 * q_);
;           const int sb = 4 * q_; v2u o;
;           o.x = pk2(sb + 0 <= t_ ? wv.x * q.x : 0.f, sb + 1 <= t_ ? wv.y * q.y : 0.f); o.y = pk2(sb + 2 <= t_ ? wv.z * q.z : 0.f, sb + 3 <= t_ ? wv.w * q.w : 0.f);
;           *(LAS v2u*)(L + SG_WOFF + t_ * SG_STR + 8 * q_) = o; } }
.LBB0_1330:
	s_and_b32 s74, s33, 0xffffff80
	s_and_b32 s83, s82, 7
	v_or_b32_e32 v128, s74, v1
	v_mad_i64_i32 v[2:3], s[0:1], v128, s77, v[108:109]
	s_lshl_b32 s84, s83, 9
	s_mov_b32 s85, s73
	v_lshl_add_u64 v[2:3], v[2:3], 0, s[84:85]
	v_lshl_add_u64 v[2:3], v[2:3], 0, v[110:111]
	v_add_co_u32_e64 v4, s[0:1], s78, v2
	s_nop 1
	v_addc_co_u32_e64 v5, s[0:1], 0, v3, s[0:1]
	s_barrier
	global_load_dwordx4 v[28:31], v[4:5], off offset:2048
	v_or_b32_e32 v126, 16, v128
	v_or_b32_e32 v124, 32, v128
	v_or_b32_e32 v122, 48, v128
	v_or_b32_e32 v120, 64, v128
	v_or_b32_e32 v118, 0x50, v128
	v_or_b32_e32 v116, 0x60, v128
	v_or_b32_e32 v114, 0x70, v128
	s_ashr_i32 s75, s74, 31
	v_ashrrev_i32_e32 v129, 31, v128
	s_lshl_b32 s72, s83, 8
	v_ashrrev_i32_e32 v127, 31, v126
	v_ashrrev_i32_e32 v125, 31, v124
	v_ashrrev_i32_e32 v123, 31, v122
	v_ashrrev_i32_e32 v121, 31, v120
	v_ashrrev_i32_e32 v119, 31, v118
	v_ashrrev_i32_e32 v117, 31, v116
	v_ashrrev_i32_e32 v115, 31, v114
	v_readlane_b32 s89, v248, 15
	s_add_i32 s82, s82, s89
	s_add_i32 s33, s33, s76
	v_mad_i64_i32 v[4:5], s[0:1], v126, s77, v[108:109]
	v_lshl_add_u64 v[4:5], v[4:5], 0, s[84:85]
	v_lshl_add_u64 v[4:5], v[4:5], 0, v[110:111]
	v_add_co_u32_e64 v26, s[0:1], s78, v4
	s_nop 1
	v_addc_co_u32_e64 v27, s[0:1], 0, v5, s[0:1]
	global_load_dwordx4 v[32:35], v[26:27], off offset:2048
	v_mad_i64_i32 v[6:7], s[0:1], v124, s77, v[108:109]
	v_lshl_add_u64 v[6:7], v[6:7], 0, s[84:85]
	v_lshl_add_u64 v[6:7], v[6:7], 0, v[110:111]
	v_add_co_u32_e64 v26, s[0:1], s78, v6
	s_nop 1
	v_addc_co_u32_e64 v27, s[0:1], 0, v7, s[0:1]
	global_load_dwordx4 v[36:39], v[26:27], off offset:2048
	v_mad_i64_i32 v[8:9], s[0:1], v122, s77, v[108:109]
	v_lshl_add_u64 v[8:9], v[8:9], 0, s[84:85]
	v_lshl_add_u64 v[8:9], v[8:9], 0, v[110:111]
	v_add_co_u32_e64 v26, s[0:1], s78, v8
	s_nop 1
	v_addc_co_u32_e64 v27, s[0:1], 0, v9, s[0:1]
	global_load_dwordx4 v[40:43], v[26:27], off offset:2048
	v_mad_i64_i32 v[10:11], s[0:1], v120, s77, v[108:109]
	v_lshl_add_u64 v[10:11], v[10:11], 0, s[84:85]
	v_lshl_add_u64 v[10:11], v[10:11], 0, v[110:111]
	v_add_co_u32_e64 v26, s[0:1], s78, v10
	s_nop 1
	v_addc_co_u32_e64 v27, s[0:1], 0, v11, s[0:1]
	global_load_dwordx4 v[44:47], v[26:27], off offset:2048
	v_mad_i64_i32 v[12:13], s[0:1], v118, s77, v[108:109]
	v_lshl_add_u64 v[12:13], v[12:13], 0, s[84:85]
	v_lshl_add_u64 v[12:13], v[12:13], 0, v[110:111]
	v_add_co_u32_e64 v26, s[0:1], s78, v12
	s_nop 1
	v_addc_co_u32_e64 v27, s[0:1], 0, v13, s[0:1]
	global_load_dwordx4 v[48:51], v[26:27], off offset:2048
	v_mad_i64_i32 v[14:15], s[0:1], v116, s77, v[108:109]
	v_lshl_add_u64 v[14:15], v[14:15], 0, s[84:85]
	v_lshl_add_u64 v[14:15], v[14:15], 0, v[110:111]
	v_add_co_u32_e64 v26, s[0:1], s78, v14
	s_nop 1
	v_addc_co_u32_e64 v27, s[0:1], 0, v15, s[0:1]
	global_load_dwordx4 v[52:55], v[26:27], off offset:2048
	v_mad_i64_i32 v[16:17], s[0:1], v114, s77, v[108:109]
	v_lshl_add_u64 v[16:17], v[16:17], 0, s[84:85]
	v_lshl_add_u64 v[16:17], v[16:17], 0, v[110:111]
	v_add_co_u32_e64 v26, s[0:1], s78, v16
	s_nop 1
	v_addc_co_u32_e64 v27, s[0:1], 0, v17, s[0:1]
	global_load_dwordx4 v[56:59], v[26:27], off offset:2048
	s_lshl_b32 s0, s83, 7
	v_or_b32_e32 v113, s0, v1
	v_lshl_add_u64 v[18:19], s[74:75], 2, v[102:103]
	global_load_dwordx4 v[18:21], v[18:19], off
	v_lshlrev_b32_e32 v100, 9, v113
	v_lshl_add_u64 v[22:23], v[104:105], 0, v[100:101]
	global_load_dwordx4 v[60:63], v[22:23], off
	v_or_b32_e32 v22, s0, v130
	v_lshlrev_b32_e32 v100, 9, v22
	v_lshl_add_u64 v[22:23], v[104:105], 0, v[100:101]
	global_load_dwordx4 v[64:67], v[22:23], off
	v_or_b32_e32 v22, s0, v131
	v_lshlrev_b32_e32 v100, 9, v22
	v_lshl_add_u64 v[22:23], v[104:105], 0, v[100:101]
	global_load_dwordx4 v[68:71], v[22:23], off
	v_or_b32_e32 v22, s0, v132
	v_lshlrev_b32_e32 v100, 9, v22
	v_lshl_add_u64 v[22:23], v[104:105], 0, v[100:101]
	global_load_dwordx4 v[72:75], v[22:23], off
	v_or_b32_e32 v22, s0, v133
	v_lshlrev_b32_e32 v100, 9, v22
	v_lshl_add_u64 v[22:23], v[104:105], 0, v[100:101]
	global_load_dwordx4 v[76:79], v[22:23], off
	v_or_b32_e32 v22, s0, v134
	v_lshlrev_b32_e32 v100, 9, v22
	v_lshl_add_u64 v[22:23], v[104:105], 0, v[100:101]
	global_load_dwordx4 v[80:83], v[22:23], off
	v_or_b32_e32 v22, s0, v135
	v_lshlrev_b32_e32 v100, 9, v22
	v_lshl_add_u64 v[22:23], v[104:105], 0, v[100:101]
	global_load_dwordx4 v[84:87], v[22:23], off
	v_or_b32_e32 v22, s0, v136
	v_lshlrev_b32_e32 v100, 9, v22
	v_lshl_add_u64 v[22:23], v[104:105], 0, v[100:101]
	global_load_dwordx4 v[88:91], v[22:23], off
	s_waitcnt vmcnt(16)
	ds_write_b128 v139, v[28:31]
	s_waitcnt vmcnt(15)
	ds_write_b128 v140, v[32:35]
	s_waitcnt vmcnt(14)
	ds_write_b128 v141, v[36:39]
	s_waitcnt vmcnt(13)
	ds_write_b128 v142, v[40:43]
	s_waitcnt vmcnt(12)
	ds_write_b128 v143, v[44:47]
	s_waitcnt vmcnt(11)
	ds_write_b128 v144, v[48:51]
	s_waitcnt vmcnt(10)
	ds_write_b128 v145, v[52:55]
	s_waitcnt vmcnt(9)
	ds_write_b128 v146, v[56:59]
	s_waitcnt vmcnt(7)
	v_mul_f32_e32 v22, v18, v60
	v_mul_f32_e32 v23, v19, v61
	v_cndmask_b32_e64 v22, v22, 0, s[70:71]
	v_cndmask_b32_e64 v23, 0, v23, s[4:5]
	v_cvt_pk_bf16_f32 v22, v22, v23
	v_mul_f32_e32 v23, v20, v62
	v_cndmask_b32_e64 v23, v23, 0, s[6:7]
	v_mul_f32_e32 v24, v21, v63
	v_cndmask_b32_e64 v24, v24, 0, s[86:87]
	v_cvt_pk_bf16_f32 v23, v23, v24
	ds_write_b64 v147, v[22:23]
	s_waitcnt vmcnt(6)
	v_mul_f32_e32 v22, v18, v64
	v_mul_f32_e32 v23, v19, v65
	v_cndmask_b32_e64 v22, v22, 0, s[90:91]
	v_cndmask_b32_e64 v23, 0, v23, s[92:93]
	v_cvt_pk_bf16_f32 v22, v22, v23
	v_mul_f32_e32 v23, v20, v66
	v_cndmask_b32_e64 v23, v23, 0, s[94:95]
	v_mul_f32_e32 v24, v21, v67
	v_cndmask_b32_e64 v24, v24, 0, s[96:97]
	v_cvt_pk_bf16_f32 v23, v23, v24
	ds_write_b64 v147, v[22:23] offset:4352
	s_waitcnt vmcnt(5)
; #define GAS __attribute__((address_space(1)))
; #define LAS __attribute__((address_space(3)))
; __device__ __forceinline__ void sgu_unit(Frame& F, int unit) {
;     ...
;     v4u uu[8];
; #pragma unroll
;     for (int i = 0; i < 8; ++i) uu[i] = *(const GAS v4u*)(F.PROJ + (size_t)(r0 + rs_ + 16 * i) * PNP + PGU + c0 + 8 * q_);
;     f32x16 acc[4];
; #pragma unroll
;     for (int tb = 0; tb < 4; ++tb)
; #pragma unroll
;         for (int r = 0; r < 16; ++r) acc[tb][r] = 0.f;
;     const LAS unsigned char* xb = L + hi * 8 * 512 + 2 * (32 * w + l31);
;     const LAS unsigned char* wa = L + SG_WOFF + l31 * SG_STR + hi * 16;
; #pragma unroll
;     for (int ks = 0; ks < 8; ++ks) {
;         v4u xw;
; #pragma unroll
;         for (int j = 0; j < 4; ++j) { const unsigned lo = *(const LAS unsigned short*)(xb + (16 * ks + 2 * j) * 512), hh = *(const LAS unsigned short*)(xb + (16 * ks + 2 * j + 1) * 512); xw[j] = lo | (hh << 16); }
;         const bf16x8 xf = __builtin_bit_cast(bf16x8, xw);
; #pragma unroll
;         for (int tb = 0; tb < 4; ++tb) if (ks < 2 * (tb + 1)) { const bf16x8 wf = *(const LAS bf16x8*)(wa + tb * 32 * SG_STR + ks * 32); acc[tb] = __builtin_amdgcn_mfma_f32_32x32x16_bf16(wf, xf, acc[tb], 0, 0, 0); } }
	v_mul_f32_e32 v22, v18, v68
	v_mul_f32_e32 v23, v19, v69
	v_cndmask_b32_e64 v22, v22, 0, vcc
	v_cndmask_b32_e64 v23, 0, v23, s[2:3]
	v_cvt_pk_bf16_f32 v22, v22, v23
	v_mul_f32_e32 v23, v20, v70
	v_cndmask_b32_e64 v23, v23, 0, s[20:21]
	v_mul_f32_e32 v24, v21, v71
	v_cndmask_b32_e64 v24, v24, 0, s[22:23]
	v_cvt_pk_bf16_f32 v23, v23, v24
	ds_write_b64 v147, v[22:23] offset:8704
	s_waitcnt vmcnt(4)
	v_mul_f32_e32 v22, v18, v72
	v_mul_f32_e32 v23, v19, v73
	v_cndmask_b32_e64 v22, v22, 0, s[24:25]
	v_cndmask_b32_e64 v23, 0, v23, s[26:27]
	v_cvt_pk_bf16_f32 v22, v22, v23
	v_mul_f32_e32 v23, v20, v74
	v_cndmask_b32_e64 v23, v23, 0, s[28:29]
	v_mul_f32_e32 v24, v21, v75
	v_cndmask_b32_e64 v24, v24, 0, s[30:31]
	v_cvt_pk_bf16_f32 v23, v23, v24
	ds_write_b64 v147, v[22:23] offset:13056
	s_waitcnt vmcnt(3)
	v_mul_f32_e32 v22, v18, v76
	v_mul_f32_e32 v23, v19, v77
	v_cndmask_b32_e64 v22, v22, 0, s[34:35]
	v_cndmask_b32_e64 v23, 0, v23, s[36:37]
	v_cvt_pk_bf16_f32 v22, v22, v23
	v_mul_f32_e32 v23, v20, v78
	v_cndmask_b32_e64 v23, v23, 0, s[38:39]
	v_mul_f32_e32 v24, v21, v79
	v_cndmask_b32_e64 v24, v24, 0, s[40:41]
	v_cvt_pk_bf16_f32 v23, v23, v24
	ds_write_b64 v147, v[22:23] offset:17408
	s_waitcnt vmcnt(2)
	v_mul_f32_e32 v22, v18, v80
	v_mul_f32_e32 v23, v19, v81
	v_cndmask_b32_e64 v22, v22, 0, s[42:43]
	v_cndmask_b32_e64 v23, 0, v23, s[66:67]
	v_cvt_pk_bf16_f32 v22, v22, v23
	v_mul_f32_e32 v23, v20, v82
	v_cndmask_b32_e64 v23, v23, 0, s[46:47]
	v_mul_f32_e32 v24, v21, v83
	v_cndmask_b32_e64 v24, v24, 0, s[48:49]
	v_cvt_pk_bf16_f32 v23, v23, v24
	ds_write_b64 v147, v[22:23] offset:21760
	s_waitcnt vmcnt(1)
	v_mul_f32_e32 v22, v18, v84
	v_mul_f32_e32 v23, v19, v85
	v_cndmask_b32_e64 v22, v22, 0, s[50:51]
	v_cndmask_b32_e64 v23, 0, v23, s[52:53]
	v_cvt_pk_bf16_f32 v22, v22, v23
	v_mul_f32_e32 v23, v20, v86
	v_cndmask_b32_e64 v23, v23, 0, s[54:55]
	v_mul_f32_e32 v24, v21, v87
	v_cndmask_b32_e64 v24, v24, 0, s[56:57]
	v_cvt_pk_bf16_f32 v23, v23, v24
	ds_write_b64 v147, v[22:23] offset:26112
	s_waitcnt vmcnt(0)
	v_add_co_u32_e64 v2, s[0:1], s79, v2
	v_mul_f32_e32 v18, v18, v88
	v_mul_f32_e32 v19, v19, v89
	v_cndmask_b32_e64 v18, v18, 0, s[58:59]
	v_cndmask_b32_e64 v19, 0, v19, s[60:61]
	v_cvt_pk_bf16_f32 v18, v18, v19
	v_mul_f32_e32 v19, v20, v90
	v_cndmask_b32_e64 v19, v19, 0, s[62:63]
	v_mul_f32_e32 v20, v21, v91
	v_addc_co_u32_e64 v3, s[0:1], 0, v3, s[0:1]
	v_cndmask_b32_e64 v20, v20, 0, s[64:65]
	v_cvt_pk_bf16_f32 v19, v19, v20
	ds_write_b64 v147, v[18:19] offset:30464
	s_waitcnt lgkmcnt(0)
	s_barrier
	global_load_dwordx4 v[94:97], v[2:3], off offset:2048
	v_add_co_u32_e64 v2, s[0:1], s79, v4
	s_nop 1
	v_addc_co_u32_e64 v3, s[0:1], 0, v5, s[0:1]
	global_load_dwordx4 v[90:93], v[2:3], off offset:2048
	v_add_co_u32_e64 v2, s[0:1], s79, v6
	s_nop 1
	v_addc_co_u32_e64 v3, s[0:1], 0, v7, s[0:1]
	global_load_dwordx4 v[86:89], v[2:3], off offset:2048
	v_add_co_u32_e64 v2, s[0:1], s79, v8
	s_nop 1
	v_addc_co_u32_e64 v3, s[0:1], 0, v9, s[0:1]
	global_load_dwordx4 v[82:85], v[2:3], off offset:2048
	v_add_co_u32_e64 v2, s[0:1], s79, v10
	s_nop 1
	v_addc_co_u32_e64 v3, s[0:1], 0, v11, s[0:1]
	global_load_dwordx4 v[78:81], v[2:3], off offset:2048
	v_add_co_u32_e64 v2, s[0:1], s79, v12
	s_nop 1
	v_addc_co_u32_e64 v3, s[0:1], 0, v13, s[0:1]
	global_load_dwordx4 v[74:77], v[2:3], off offset:2048
	v_add_co_u32_e64 v2, s[0:1], s79, v14
	s_nop 1
	v_addc_co_u32_e64 v3, s[0:1], 0, v15, s[0:1]
	global_load_dwordx4 v[70:73], v[2:3], off offset:2048
	v_add_co_u32_e64 v2, s[0:1], s79, v16
	s_nop 1
	v_addc_co_u32_e64 v3, s[0:1], 0, v17, s[0:1]
	global_load_dwordx4 v[66:69], v[2:3], off offset:2048
	s_lshl_b32 s0, s83, 10
	s_mov_b32 s1, s73
	s_cmpk_gt_i32 s82, 0x1ff
	ds_read_u16 v188, v137
	ds_read_u16 v189, v137 offset:512
	ds_read_u16 v190, v137 offset:1024
	ds_read_u16 v191, v137 offset:1536
	ds_read_u16 v192, v137 offset:2048
	ds_read_u16 v193, v137 offset:2560
	ds_read_u16 v194, v137 offset:3072
	ds_read_u16 v195, v137 offset:3584
	ds_read_b128 v[212:215], v148
	ds_read_b128 v[216:219], v148 offset:8704
	ds_read_b128 v[220:223], v148 offset:17408
	ds_read_b128 v[224:227], v148 offset:26112
	ds_read_u16 v196, v137 offset:8192
	ds_read_u16 v197, v137 offset:8704
	ds_read_u16 v198, v137 offset:9216
	ds_read_u16 v199, v137 offset:9728
	ds_read_u16 v200, v137 offset:10240
	ds_read_u16 v201, v137 offset:10752
	ds_read_u16 v202, v137 offset:11264
	ds_read_u16 v203, v137 offset:11776
	ds_read_b128 v[228:231], v148 offset:32
	ds_read_b128 v[232:235], v148 offset:8736
	ds_read_b128 v[236:239], v148 offset:17440
	ds_read_b128 v[240:243], v148 offset:26144
	s_waitcnt lgkmcnt(12)
	v_lshl_or_b32 v204, v189, 16, v188
	v_lshl_or_b32 v205, v191, 16, v190
	v_lshl_or_b32 v206, v193, 16, v192
	v_lshl_or_b32 v207, v195, 16, v194
	s_nop 1
	v_mfma_f32_32x32x16_bf16 v[50:65], v[212:215], v[204:207], 0
	v_mfma_f32_32x32x16_bf16 v[34:49], v[216:219], v[204:207], 0
	v_mfma_f32_32x32x16_bf16 v[18:33], v[220:223], v[204:207], 0
	v_mfma_f32_32x32x16_bf16 v[2:17], v[224:227], v[204:207], 0
	ds_read_u16 v188, v137 offset:16384
	ds_read_u16 v189, v137 offset:16896
	ds_read_u16 v190, v137 offset:17408
	ds_read_u16 v191, v137 offset:17920
	ds_read_u16 v192, v137 offset:18432
	ds_read_u16 v193, v137 offset:18944
	ds_read_u16 v194, v137 offset:19456
	ds_read_u16 v195, v137 offset:19968
	ds_read_b128 v[216:219], v148 offset:8768
	ds_read_b128 v[220:223], v148 offset:17472
	ds_read_b128 v[224:227], v148 offset:26176
	s_waitcnt lgkmcnt(11)
; #define LAS __attribute__((address_space(3)))
; #define LDS_WAIT() asm volatile("s_waitcnt lgkmcnt(0)" ::: "memory")
; __device__ __forceinline__ unsigned f2bf(float f) { unsigned u = __builtin_bit_cast(unsigned, f); return (u + 0x7fffu + ((u >> 16) & 1u)) >> 16; }
; __device__ __forceinline__ void sgu_unit(Frame& F, int unit) {
;     ...
; #pragma unroll
;     for (int ks = 0; ks < 8; ++ks) {
;         v4u xw;
; #pragma unroll
;         for (int j = 0; j < 4; ++j) { const unsigned lo = *(const LAS unsigned short*)(xb + (16 * ks + 2 * j) * 512), hh = *(const LAS unsigned short*)(xb + (16 * ks + 2 * j + 1) * 512); xw[j] = lo | (hh << 16); }
;         const bf16x8 xf = __builtin_bit_cast(bf16x8, xw);
; #pragma unroll
;         for (int tb = 0; tb < 4; ++tb) if (ks < 2 * (tb + 1)) { const bf16x8 wf = *(const LAS bf16x8*)(wa + tb * 32 * SG_STR + ks * 32); acc[tb] = __builtin_amdgcn_mfma_f32_32x32x16_bf16(wf, xf, acc[tb], 0, 0, 0); } }
;     LDS_WAIT(); __builtin_amdgcn_s_barrier(); asm volatile("" ::: "memory");
;     { const int cl = 32 * w + l31;
; #pragma unroll
;       for (int tb = 0; tb < 4; ++tb)
; #pragma unroll
;           for (int r = 0; r < 16; ++r) { const int t = 32 * tb + (r & 3) + 8 * (r >> 2) + 4 * hi; *(LAS unsigned short*)(L + t * 512 + 2 * cl) = (unsigned short)f2bf(acc[tb][r]); } }
	v_lshl_or_b32 v208, v197, 16, v196
	v_lshl_or_b32 v209, v199, 16, v198
	v_lshl_or_b32 v210, v201, 16, v200
	v_lshl_or_b32 v211, v203, 16, v202
	s_nop 1
	v_mfma_f32_32x32x16_bf16 v[50:65], v[228:231], v[208:211], v[50:65]
	v_mfma_f32_32x32x16_bf16 v[34:49], v[232:235], v[208:211], v[34:49]
	v_mfma_f32_32x32x16_bf16 v[18:33], v[236:239], v[208:211], v[18:33]
	v_mfma_f32_32x32x16_bf16 v[2:17], v[240:243], v[208:211], v[2:17]
	ds_read_u16 v196, v137 offset:24576
	ds_read_u16 v197, v137 offset:25088
	ds_read_u16 v198, v137 offset:25600
	ds_read_u16 v199, v137 offset:26112
	ds_read_u16 v200, v137 offset:26624
	ds_read_u16 v201, v137 offset:27136
	ds_read_u16 v202, v137 offset:27648
	ds_read_u16 v203, v137 offset:28160
	ds_read_b128 v[232:235], v148 offset:8800
	ds_read_b128 v[236:239], v148 offset:17504
	ds_read_b128 v[240:243], v148 offset:26208
	s_waitcnt lgkmcnt(11)
	v_lshl_or_b32 v204, v189, 16, v188
	v_lshl_or_b32 v205, v191, 16, v190
	v_lshl_or_b32 v206, v193, 16, v192
	v_lshl_or_b32 v207, v195, 16, v194
	s_nop 1
	v_mfma_f32_32x32x16_bf16 v[34:49], v[216:219], v[204:207], v[34:49]
	v_mfma_f32_32x32x16_bf16 v[18:33], v[220:223], v[204:207], v[18:33]
	v_mfma_f32_32x32x16_bf16 v[2:17], v[224:227], v[204:207], v[2:17]
	ds_read_u16 v188, v137 offset:32768
	ds_read_u16 v189, v137 offset:33280
	ds_read_u16 v190, v137 offset:33792
	ds_read_u16 v191, v137 offset:34304
	ds_read_u16 v192, v137 offset:34816
	ds_read_u16 v193, v137 offset:35328
	ds_read_u16 v194, v137 offset:35840
	ds_read_u16 v195, v137 offset:36352
	ds_read_b128 v[220:223], v148 offset:17536
	ds_read_b128 v[224:227], v148 offset:26240
	s_waitcnt lgkmcnt(10)
	v_lshl_or_b32 v208, v197, 16, v196
	v_lshl_or_b32 v209, v199, 16, v198
	v_lshl_or_b32 v210, v201, 16, v200
	v_lshl_or_b32 v211, v203, 16, v202
	s_nop 1
	v_mfma_f32_32x32x16_bf16 v[34:49], v[232:235], v[208:211], v[34:49]
	v_mfma_f32_32x32x16_bf16 v[18:33], v[236:239], v[208:211], v[18:33]
	v_mfma_f32_32x32x16_bf16 v[2:17], v[240:243], v[208:211], v[2:17]
	ds_read_u16 v196, v137 offset:40960
	ds_read_u16 v197, v137 offset:41472
	ds_read_u16 v198, v137 offset:41984
	ds_read_u16 v199, v137 offset:42496
	ds_read_u16 v200, v137 offset:43008
	ds_read_u16 v201, v137 offset:43520
	ds_read_u16 v202, v137 offset:44032
	ds_read_u16 v203, v137 offset:44544
	ds_read_b128 v[236:239], v148 offset:17568
	ds_read_b128 v[240:243], v148 offset:26272
	s_waitcnt lgkmcnt(10)
	v_lshl_or_b32 v204, v189, 16, v188
	v_lshl_or_b32 v205, v191, 16, v190
	v_lshl_or_b32 v206, v193, 16, v192
	v_lshl_or_b32 v207, v195, 16, v194
	s_nop 1
	v_mfma_f32_32x32x16_bf16 v[18:33], v[220:223], v[204:207], v[18:33]
	v_mfma_f32_32x32x16_bf16 v[2:17], v[224:227], v[204:207], v[2:17]
	ds_read_u16 v188, v137 offset:49152
	ds_read_u16 v189, v137 offset:49664
	ds_read_u16 v190, v137 offset:50176
	ds_read_u16 v191, v137 offset:50688
	ds_read_u16 v192, v137 offset:51200
	ds_read_u16 v193, v137 offset:51712
	ds_read_u16 v194, v137 offset:52224
	ds_read_u16 v195, v137 offset:52736
	ds_read_b128 v[224:227], v148 offset:26304
	s_waitcnt lgkmcnt(9)
	v_lshl_or_b32 v208, v197, 16, v196
	v_lshl_or_b32 v209, v199, 16, v198
	v_lshl_or_b32 v210, v201, 16, v200
	v_lshl_or_b32 v211, v203, 16, v202
	s_nop 1
	v_mfma_f32_32x32x16_bf16 v[18:33], v[236:239], v[208:211], v[18:33]
	v_mfma_f32_32x32x16_bf16 v[2:17], v[240:243], v[208:211], v[2:17]
	s_waitcnt lgkmcnt(0)
	v_lshl_or_b32 v204, v189, 16, v188
	v_lshl_or_b32 v205, v191, 16, v190
	v_lshl_or_b32 v206, v193, 16, v192
	v_lshl_or_b32 v207, v195, 16, v194
	s_nop 1
	v_mfma_f32_32x32x16_bf16 v[2:17], v[224:227], v[204:207], v[2:17]
	ds_read_u16 v100, v137 offset:57344
	ds_read_u16 v150, v137 offset:57856
	s_waitcnt lgkmcnt(0)
	v_lshl_or_b32 v150, v150, 16, v100
	ds_read_u16 v100, v137 offset:58368
	ds_read_u16 v151, v137 offset:58880
	s_waitcnt lgkmcnt(0)
	v_lshl_or_b32 v151, v151, 16, v100
	ds_read_u16 v100, v137 offset:59392
	ds_read_u16 v152, v137 offset:59904
	s_waitcnt lgkmcnt(0)
	v_lshl_or_b32 v152, v152, 16, v100
	ds_read_u16 v100, v137 offset:60416
	ds_read_u16 v153, v137 offset:60928
	ds_read_b128 v[154:157], v148 offset:26336
	s_waitcnt lgkmcnt(0)
	s_barrier
	s_waitcnt lgkmcnt(1)
	v_lshl_or_b32 v153, v153, 16, v100
	v_bfe_u32 v100, v50, 16, 1
	v_add3_u32 v50, v50, v100, s80
	ds_write_b16_d16_hi v138, v50
	v_bfe_u32 v50, v51, 16, 1
	v_add3_u32 v50, v51, v50, s80
	ds_write_b16_d16_hi v138, v50 offset:512
	v_bfe_u32 v50, v52, 16, 1
	v_add3_u32 v50, v52, v50, s80
	ds_write_b16_d16_hi v138, v50 offset:1024
	v_bfe_u32 v50, v53, 16, 1
	v_add3_u32 v50, v53, v50, s80
	ds_write_b16_d16_hi v138, v50 offset:1536
	v_bfe_u32 v50, v54, 16, 1
	v_add3_u32 v50, v54, v50, s80
	ds_write_b16_d16_hi v138, v50 offset:4096
	v_bfe_u32 v50, v55, 16, 1
	v_add3_u32 v50, v55, v50, s80
	ds_write_b16_d16_hi v138, v50 offset:4608
	v_bfe_u32 v50, v56, 16, 1
	v_add3_u32 v50, v56, v50, s80
	ds_write_b16_d16_hi v138, v50 offset:5120
	v_bfe_u32 v50, v57, 16, 1
	v_add3_u32 v50, v57, v50, s80
	ds_write_b16_d16_hi v138, v50 offset:5632
	v_bfe_u32 v50, v58, 16, 1
	v_add3_u32 v50, v58, v50, s80
	ds_write_b16_d16_hi v138, v50 offset:8192
	v_bfe_u32 v50, v59, 16, 1
	v_add3_u32 v50, v59, v50, s80
	ds_write_b16_d16_hi v138, v50 offset:8704
	v_bfe_u32 v50, v60, 16, 1
	v_add3_u32 v50, v60, v50, s80
	ds_write_b16_d16_hi v138, v50 offset:9216
	v_bfe_u32 v50, v61, 16, 1
	v_add3_u32 v50, v61, v50, s80
	ds_write_b16_d16_hi v138, v50 offset:9728
	v_bfe_u32 v50, v62, 16, 1
	v_add3_u32 v50, v62, v50, s80
	ds_write_b16_d16_hi v138, v50 offset:12288
	v_bfe_u32 v50, v63, 16, 1
	v_add3_u32 v50, v63, v50, s80
	ds_write_b16_d16_hi v138, v50 offset:12800
	v_bfe_u32 v50, v64, 16, 1
; #define GAS __attribute__((address_space(1)))
; #define LAS __attribute__((address_space(3)))
; #define LDS_WAIT() asm volatile("s_waitcnt lgkmcnt(0)" ::: "memory")
; __device__ __forceinline__ unsigned f2bf(float f) { unsigned u = __builtin_bit_cast(unsigned, f); return (u + 0x7fffu + ((u >> 16) & 1u)) >> 16; }
; __device__ __forceinline__ void sgu_unit(Frame& F, int unit) {
;     ...
;     LDS_WAIT(); __builtin_amdgcn_s_barrier(); asm volatile("" ::: "memory");
;     { const int cl = 32 * w + l31;
; #pragma unroll
;       for (int tb = 0; tb < 4; ++tb)
; #pragma unroll
;           for (int r = 0; r < 16; ++r) { const int t = 32 * tb + (r & 3) + 8 * (r >> 2) + 4 * hi; *(LAS unsigned short*)(L + t * 512 + 2 * cl) = (unsigned short)f2bf(acc[tb][r]); } }
;     const f32x4 g0 = *(const GAS f32x4*)(F.sgg + c0 + 8 * q_), g1 = *(const GAS f32x4*)(F.sgg + c0 + 8 * q_ + 4);
;     LDS_WAIT(); __builtin_amdgcn_s_barrier(); asm volatile("" ::: "memory");
	v_add3_u32 v50, v64, v50, s80
	ds_write_b16_d16_hi v138, v50 offset:13312
	v_bfe_u32 v50, v65, 16, 1
	v_add3_u32 v50, v65, v50, s80
	ds_write_b16_d16_hi v138, v50 offset:13824
	v_bfe_u32 v50, v34, 16, 1
	v_add3_u32 v34, v34, v50, s80
	ds_write_b16_d16_hi v138, v34 offset:16384
	v_bfe_u32 v34, v35, 16, 1
	v_add3_u32 v34, v35, v34, s80
	ds_write_b16_d16_hi v138, v34 offset:16896
	v_bfe_u32 v34, v36, 16, 1
	v_add3_u32 v34, v36, v34, s80
	ds_write_b16_d16_hi v138, v34 offset:17408
	v_bfe_u32 v34, v37, 16, 1
	v_add3_u32 v34, v37, v34, s80
	ds_write_b16_d16_hi v138, v34 offset:17920
	v_bfe_u32 v34, v38, 16, 1
	v_add3_u32 v34, v38, v34, s80
	ds_write_b16_d16_hi v138, v34 offset:20480
	v_bfe_u32 v34, v39, 16, 1
	v_add3_u32 v34, v39, v34, s80
	ds_write_b16_d16_hi v138, v34 offset:20992
	v_bfe_u32 v34, v40, 16, 1
	v_add3_u32 v34, v40, v34, s80
	ds_write_b16_d16_hi v138, v34 offset:21504
	v_bfe_u32 v34, v41, 16, 1
	v_add3_u32 v34, v41, v34, s80
	ds_write_b16_d16_hi v138, v34 offset:22016
	v_bfe_u32 v34, v42, 16, 1
	v_add3_u32 v34, v42, v34, s80
	ds_write_b16_d16_hi v138, v34 offset:24576
	v_bfe_u32 v34, v43, 16, 1
	v_add3_u32 v34, v43, v34, s80
	ds_write_b16_d16_hi v138, v34 offset:25088
	v_bfe_u32 v34, v44, 16, 1
	v_add3_u32 v34, v44, v34, s80
	ds_write_b16_d16_hi v138, v34 offset:25600
	v_bfe_u32 v34, v45, 16, 1
	v_add3_u32 v34, v45, v34, s80
	ds_write_b16_d16_hi v138, v34 offset:26112
	v_bfe_u32 v34, v46, 16, 1
	v_add3_u32 v34, v46, v34, s80
	ds_write_b16_d16_hi v138, v34 offset:28672
	v_bfe_u32 v34, v47, 16, 1
	v_add3_u32 v34, v47, v34, s80
	ds_write_b16_d16_hi v138, v34 offset:29184
	v_bfe_u32 v34, v48, 16, 1
	v_add3_u32 v34, v48, v34, s80
	ds_write_b16_d16_hi v138, v34 offset:29696
	v_bfe_u32 v34, v49, 16, 1
	v_add3_u32 v34, v49, v34, s80
	ds_write_b16_d16_hi v138, v34 offset:30208
	v_bfe_u32 v34, v18, 16, 1
	v_add3_u32 v18, v18, v34, s80
	ds_write_b16_d16_hi v138, v18 offset:32768
	v_bfe_u32 v18, v19, 16, 1
	v_add3_u32 v18, v19, v18, s80
	ds_write_b16_d16_hi v138, v18 offset:33280
	v_bfe_u32 v18, v20, 16, 1
	v_add3_u32 v18, v20, v18, s80
	ds_write_b16_d16_hi v138, v18 offset:33792
	v_bfe_u32 v18, v21, 16, 1
	v_add3_u32 v18, v21, v18, s80
	ds_write_b16_d16_hi v138, v18 offset:34304
	v_bfe_u32 v18, v22, 16, 1
	v_add3_u32 v18, v22, v18, s80
	ds_write_b16_d16_hi v138, v18 offset:36864
	v_bfe_u32 v18, v23, 16, 1
	v_add3_u32 v18, v23, v18, s80
	ds_write_b16_d16_hi v138, v18 offset:37376
	v_bfe_u32 v18, v24, 16, 1
	v_add3_u32 v18, v24, v18, s80
	ds_write_b16_d16_hi v138, v18 offset:37888
	v_bfe_u32 v18, v25, 16, 1
	v_add3_u32 v18, v25, v18, s80
	ds_write_b16_d16_hi v138, v18 offset:38400
	v_bfe_u32 v18, v26, 16, 1
	v_add3_u32 v18, v26, v18, s80
	ds_write_b16_d16_hi v138, v18 offset:40960
	v_bfe_u32 v18, v27, 16, 1
	v_add3_u32 v18, v27, v18, s80
	ds_write_b16_d16_hi v138, v18 offset:41472
	v_bfe_u32 v18, v28, 16, 1
	v_add3_u32 v18, v28, v18, s80
	ds_write_b16_d16_hi v138, v18 offset:41984
	v_bfe_u32 v18, v29, 16, 1
	v_add3_u32 v18, v29, v18, s80
	s_waitcnt lgkmcnt(14)
	v_mfma_f32_32x32x16_bf16 v[2:17], v[154:157], v[150:153], v[2:17]
	ds_write_b16_d16_hi v138, v18 offset:42496
	v_bfe_u32 v18, v30, 16, 1
	v_add3_u32 v18, v30, v18, s80
	ds_write_b16_d16_hi v138, v18 offset:45056
	v_bfe_u32 v18, v31, 16, 1
	v_add3_u32 v18, v31, v18, s80
	ds_write_b16_d16_hi v138, v18 offset:45568
	v_bfe_u32 v18, v32, 16, 1
	v_add3_u32 v18, v32, v18, s80
	ds_write_b16_d16_hi v138, v18 offset:46080
	v_bfe_u32 v18, v33, 16, 1
	v_add3_u32 v18, v33, v18, s80
	ds_write_b16_d16_hi v138, v18 offset:46592
	v_bfe_u32 v18, v2, 16, 1
	v_add3_u32 v2, v2, v18, s80
	ds_write_b16_d16_hi v138, v2 offset:49152
	v_bfe_u32 v2, v3, 16, 1
	v_add3_u32 v2, v3, v2, s80
	ds_write_b16_d16_hi v138, v2 offset:49664
	v_bfe_u32 v2, v4, 16, 1
	v_add3_u32 v2, v4, v2, s80
	ds_write_b16_d16_hi v138, v2 offset:50176
	v_bfe_u32 v2, v5, 16, 1
	v_add3_u32 v2, v5, v2, s80
	ds_write_b16_d16_hi v138, v2 offset:50688
	v_bfe_u32 v2, v6, 16, 1
	v_add3_u32 v2, v6, v2, s80
	ds_write_b16_d16_hi v138, v2 offset:53248
	v_bfe_u32 v2, v7, 16, 1
	v_add3_u32 v2, v7, v2, s80
	ds_write_b16_d16_hi v138, v2 offset:53760
	v_bfe_u32 v2, v8, 16, 1
	v_add3_u32 v2, v8, v2, s80
	ds_write_b16_d16_hi v138, v2 offset:54272
	v_bfe_u32 v2, v9, 16, 1
	v_add3_u32 v2, v9, v2, s80
	ds_write_b16_d16_hi v138, v2 offset:54784
	v_bfe_u32 v2, v10, 16, 1
	v_add3_u32 v2, v10, v2, s80
	ds_write_b16_d16_hi v138, v2 offset:57344
	v_bfe_u32 v2, v11, 16, 1
	v_add3_u32 v2, v11, v2, s80
	ds_write_b16_d16_hi v138, v2 offset:57856
	v_bfe_u32 v2, v12, 16, 1
	v_add3_u32 v2, v12, v2, s80
	ds_write_b16_d16_hi v138, v2 offset:58368
	v_bfe_u32 v2, v13, 16, 1
	v_add3_u32 v2, v13, v2, s80
	ds_write_b16_d16_hi v138, v2 offset:58880
	v_bfe_u32 v2, v14, 16, 1
	v_add3_u32 v2, v14, v2, s80
	ds_write_b16_d16_hi v138, v2 offset:61440
	v_bfe_u32 v2, v15, 16, 1
	v_add3_u32 v2, v15, v2, s80
	ds_write_b16_d16_hi v138, v2 offset:61952
	v_bfe_u32 v2, v16, 16, 1
	v_add3_u32 v2, v16, v2, s80
	ds_write_b16_d16_hi v138, v2 offset:62464
	v_bfe_u32 v2, v17, 16, 1
	v_add3_u32 v2, v17, v2, s80
	ds_write_b16_d16_hi v138, v2 offset:62976
	v_lshl_add_u64 v[6:7], v[106:107], 0, s[0:1]
	global_load_dwordx4 v[2:5], v[6:7], off offset:16
	s_nop 0
	global_load_dwordx4 v[6:9], v[6:7], off
	s_waitcnt lgkmcnt(0)
	s_barrier
; #define GAS __attribute__((address_space(1)))
; #define LAS __attribute__((address_space(3)))
; __device__ __forceinline__ void sgu_unit(Frame& F, int unit) {
;     ...
; #pragma unroll
;     for (int i = 0; i < 8; ++i) { const v4u fw = *(const LAS v4u*)(L + (rs_ + 16 * i) * 512 + q_ * 16); const float bb = F.sgb[g * GMC + rs_ + 16 * i]; v2u o;
;         o.x = pk4_fp8(S_YB * bflo(uu[i].x) * (bflo(fw.x) * g0.x + bb), S_YB * bfhi(uu[i].x) * (bfhi(fw.x) * g0.y + bb), S_YB * bflo(uu[i].y) * (bflo(fw.y) * g0.z + bb), S_YB * bfhi(uu[i].y) * (bfhi(fw.y) * g0.w + bb));
;         o.y = pk4_fp8(S_YB * bflo(uu[i].z) * (bflo(fw.z) * g1.x + bb), S_YB * bfhi(uu[i].z) * (bfhi(fw.z) * g1.y + bb), S_YB * bflo(uu[i].w) * (bflo(fw.w) * g1.z + bb), S_YB * bfhi(uu[i].w) * (bfhi(fw.w) * g1.w + bb));
;         *(GAS v2u*)((unsigned char*)F.YA + (size_t)(r0 + rs_ + 16 * i) * (2 * ATTW) + ATTW + c0 + 8 * q_) = o; }
	v_lshlrev_b32_e32 v20, 2, v113
	global_load_dword v240, v20, s[8:9]
	global_load_dword v241, v20, s[8:9] offset:64
	global_load_dword v242, v20, s[8:9] offset:128
	global_load_dword v243, v20, s[8:9] offset:192
	global_load_dword v244, v20, s[8:9] offset:256
	global_load_dword v245, v20, s[8:9] offset:320
	global_load_dword v246, v20, s[8:9] offset:384
	global_load_dword v247, v20, s[8:9] offset:448
	ds_read_b128 v[10:13], v139
	s_waitcnt vmcnt(17)
	v_lshlrev_b32_e32 v14, 16, v94
	v_lshlrev_b32_e32 v16, 16, v95
	v_lshlrev_b32_e32 v22, 16, v97
	s_waitcnt lgkmcnt(0)
	v_lshlrev_b32_e32 v15, 16, v10
	v_lshlrev_b32_e32 v17, 16, v11
	v_and_b32_e32 v11, 0xffff0000, v11
	v_lshlrev_b32_e32 v23, 16, v13
	v_and_b32_e32 v13, 0xffff0000, v13
	s_waitcnt vmcnt(8)
	v_mov_b32_e32 v113, v6
	v_pk_mul_f32 v[14:15], v[112:113], v[14:15]
	s_waitcnt vmcnt(7)
	v_mov_b32_e32 v19, v240
	v_add_f32_e32 v6, v19, v15
	v_mul_f32_e32 v18, v14, v6
	v_and_b32_e32 v15, 0xffff0000, v10
	v_and_b32_e32 v14, 0xffff0000, v94
	v_mov_b32_e32 v6, v112
	v_pk_mul_f32 v[14:15], v[6:7], v[14:15]
	s_nop 0
	v_add_f32_e32 v10, v19, v15
	v_mul_f32_e32 v21, v14, v10
	v_mov_b32_e32 v14, v112
	v_mov_b32_e32 v15, v8
	v_pk_mul_f32 v[16:17], v[14:15], v[16:17]
	v_and_b32_e32 v10, 0xffff0000, v95
	v_add_f32_e32 v8, v19, v17
	v_mul_f32_e32 v16, v16, v8
	v_mov_b32_e32 v8, v112
	v_pk_mul_f32 v[10:11], v[8:9], v[10:11]
	v_med3_f32 v17, v21, s81, v149
	v_add_f32_e32 v11, v19, v11
	v_mul_f32_e32 v10, v10, v11
	v_med3_f32 v11, v18, s81, v149
	v_mov_b32_e32 v18, v101
	v_cvt_pk_fp8_f32 v18, v11, v17
	v_med3_f32 v11, v16, s81, v149
	v_med3_f32 v10, v10, s81, v149
	v_lshlrev_b32_e32 v16, 16, v96
	v_cvt_pk_fp8_f32 v18, v11, v10 op_sel:[0,0,1]
	v_lshlrev_b32_e32 v17, 16, v12
	v_mov_b32_e32 v10, v112
	v_mov_b32_e32 v11, v2
	v_pk_mul_f32 v[16:17], v[10:11], v[16:17]
	s_nop 0
	v_add_f32_e32 v2, v19, v17
	v_mul_f32_e32 v21, v16, v2
	v_and_b32_e32 v17, 0xffff0000, v12
	v_and_b32_e32 v16, 0xffff0000, v96
	v_mov_b32_e32 v2, v112
	v_pk_mul_f32 v[16:17], v[2:3], v[16:17]
	s_nop 0
	v_add_f32_e32 v12, v19, v17
	v_mul_f32_e32 v24, v16, v12
	v_mov_b32_e32 v16, v112
	v_mov_b32_e32 v17, v4
	v_pk_mul_f32 v[22:23], v[16:17], v[22:23]
	v_and_b32_e32 v12, 0xffff0000, v97
	v_add_f32_e32 v4, v19, v23
	v_mul_f32_e32 v22, v22, v4
	v_mov_b32_e32 v4, v112
	v_pk_mul_f32 v[12:13], v[4:5], v[12:13]
	s_nop 0
	v_add_f32_e32 v13, v19, v13
	v_mul_f32_e32 v12, v12, v13
	v_med3_f32 v13, v21, s81, v149
	v_med3_f32 v21, v24, s81, v149
	v_mov_b32_e32 v19, v101
	v_cvt_pk_fp8_f32 v19, v13, v21
	v_med3_f32 v13, v22, s81, v149
	v_med3_f32 v12, v12, s81, v149
	ds_read_b128 v[22:25], v140
	v_cvt_pk_fp8_f32 v19, v13, v12 op_sel:[0,0,1]
	v_lshlrev_b64 v[12:13], 12, v[128:129]
	v_lshl_add_u64 v[12:13], s[68:69], 0, v[12:13]
	v_lshl_add_u64 v[12:13], v[12:13], 0, s[72:73]
	v_lshl_add_u64 v[12:13], v[12:13], 0, v[98:99]
	global_store_dwordx2 v[12:13], v[18:19], off offset:2048
	v_lshlrev_b32_e32 v12, 16, v90
	s_waitcnt lgkmcnt(0)
	v_lshlrev_b32_e32 v13, 16, v22
	v_pk_mul_f32 v[12:13], v[112:113], v[12:13]
	s_waitcnt vmcnt(7)
	v_mov_b32_e32 v21, v241
	v_add_f32_e32 v13, v21, v13
	v_mul_f32_e32 v18, v12, v13
	v_and_b32_e32 v13, 0xffff0000, v22
	v_and_b32_e32 v12, 0xffff0000, v90
	v_pk_mul_f32 v[12:13], v[6:7], v[12:13]
	v_med3_f32 v18, v18, s81, v149
	v_add_f32_e32 v13, v21, v13
	v_mul_f32_e32 v19, v12, v13
	v_lshlrev_b32_e32 v12, 16, v91
	v_lshlrev_b32_e32 v13, 16, v23
	v_pk_mul_f32 v[12:13], v[14:15], v[12:13]
	v_med3_f32 v19, v19, s81, v149
	v_add_f32_e32 v13, v21, v13
	v_mul_f32_e32 v22, v12, v13
	v_and_b32_e32 v13, 0xffff0000, v23
	v_and_b32_e32 v12, 0xffff0000, v91
	v_pk_mul_f32 v[12:13], v[8:9], v[12:13]
	s_nop 0
	v_add_f32_e32 v13, v21, v13
	v_mul_f32_e32 v13, v12, v13
	v_mov_b32_e32 v12, v101
	v_cvt_pk_fp8_f32 v12, v18, v19
	v_med3_f32 v18, v22, s81, v149
	v_med3_f32 v13, v13, s81, v149
	v_lshlrev_b32_e32 v19, 16, v24
	v_cvt_pk_fp8_f32 v12, v18, v13 op_sel:[0,0,1]
	v_lshlrev_b32_e32 v18, 16, v92
	v_pk_mul_f32 v[18:19], v[10:11], v[18:19]
	s_nop 0
	v_add_f32_e32 v13, v21, v19
	v_mul_f32_e32 v13, v18, v13
	v_and_b32_e32 v19, 0xffff0000, v24
	v_and_b32_e32 v18, 0xffff0000, v92
	v_pk_mul_f32 v[18:19], v[2:3], v[18:19]
	s_nop 0
	v_add_f32_e32 v19, v21, v19
	v_mul_f32_e32 v22, v18, v19
	v_lshlrev_b32_e32 v18, 16, v93
	v_lshlrev_b32_e32 v19, 16, v25
	v_pk_mul_f32 v[18:19], v[16:17], v[18:19]
	s_nop 0
	v_add_f32_e32 v19, v21, v19
	v_mul_f32_e32 v23, v18, v19
	v_and_b32_e32 v19, 0xffff0000, v25
	v_and_b32_e32 v18, 0xffff0000, v93
	v_pk_mul_f32 v[18:19], v[4:5], v[18:19]
	s_nop 0
	v_add_f32_e32 v19, v21, v19
	v_mul_f32_e32 v18, v18, v19
	v_med3_f32 v19, v13, s81, v149
	v_med3_f32 v21, v22, s81, v149
	v_mov_b32_e32 v13, v101
	v_cvt_pk_fp8_f32 v13, v19, v21
	v_med3_f32 v19, v23, s81, v149
	v_med3_f32 v18, v18, s81, v149
	ds_read_b128 v[22:25], v141
	v_cvt_pk_fp8_f32 v13, v19, v18 op_sel:[0,0,1]
	v_lshlrev_b64 v[18:19], 12, v[126:127]
	v_lshl_add_u64 v[18:19], s[68:69], 0, v[18:19]
	v_lshl_add_u64 v[18:19], v[18:19], 0, s[72:73]
	v_lshl_add_u64 v[18:19], v[18:19], 0, v[98:99]
	global_store_dwordx2 v[18:19], v[12:13], off offset:2048
	v_lshlrev_b32_e32 v12, 16, v86
	s_waitcnt lgkmcnt(0)
	v_lshlrev_b32_e32 v13, 16, v22
	v_pk_mul_f32 v[12:13], v[112:113], v[12:13]
	s_waitcnt vmcnt(7)
; #define GAS __attribute__((address_space(1)))
; #define LAS __attribute__((address_space(3)))
; __device__ __forceinline__ void sgu_unit(Frame& F, int unit) {
;     ...
; #pragma unroll
;     for (int i = 0; i < 8; ++i) { const v4u fw = *(const LAS v4u*)(L + (rs_ + 16 * i) * 512 + q_ * 16); const float bb = F.sgb[g * GMC + rs_ + 16 * i]; v2u o;
;         o.x = pk4_fp8(S_YB * bflo(uu[i].x) * (bflo(fw.x) * g0.x + bb), S_YB * bfhi(uu[i].x) * (bfhi(fw.x) * g0.y + bb), S_YB * bflo(uu[i].y) * (bflo(fw.y) * g0.z + bb), S_YB * bfhi(uu[i].y) * (bfhi(fw.y) * g0.w + bb));
;         o.y = pk4_fp8(S_YB * bflo(uu[i].z) * (bflo(fw.z) * g1.x + bb), S_YB * bfhi(uu[i].z) * (bfhi(fw.z) * g1.y + bb), S_YB * bflo(uu[i].w) * (bflo(fw.w) * g1.z + bb), S_YB * bfhi(uu[i].w) * (bfhi(fw.w) * g1.w + bb));
;         *(GAS v2u*)((unsigned char*)F.YA + (size_t)(r0 + rs_ + 16 * i) * (2 * ATTW) + ATTW + c0 + 8 * q_) = o; }
	v_mov_b32_e32 v21, v242
	v_add_f32_e32 v13, v21, v13
	v_mul_f32_e32 v18, v12, v13
	v_and_b32_e32 v13, 0xffff0000, v22
	v_and_b32_e32 v12, 0xffff0000, v86
	v_pk_mul_f32 v[12:13], v[6:7], v[12:13]
	v_med3_f32 v18, v18, s81, v149
	v_add_f32_e32 v13, v21, v13
	v_mul_f32_e32 v19, v12, v13
	v_lshlrev_b32_e32 v12, 16, v87
	v_lshlrev_b32_e32 v13, 16, v23
	v_pk_mul_f32 v[12:13], v[14:15], v[12:13]
	v_med3_f32 v19, v19, s81, v149
	v_add_f32_e32 v13, v21, v13
	v_mul_f32_e32 v22, v12, v13
	v_and_b32_e32 v13, 0xffff0000, v23
	v_and_b32_e32 v12, 0xffff0000, v87
	v_pk_mul_f32 v[12:13], v[8:9], v[12:13]
	s_nop 0
	v_add_f32_e32 v13, v21, v13
	v_mul_f32_e32 v13, v12, v13
	v_mov_b32_e32 v12, v101
	v_cvt_pk_fp8_f32 v12, v18, v19
	v_med3_f32 v18, v22, s81, v149
	v_med3_f32 v13, v13, s81, v149
	v_lshlrev_b32_e32 v19, 16, v24
	v_cvt_pk_fp8_f32 v12, v18, v13 op_sel:[0,0,1]
	v_lshlrev_b32_e32 v18, 16, v88
	v_pk_mul_f32 v[18:19], v[10:11], v[18:19]
	s_nop 0
	v_add_f32_e32 v13, v21, v19
	v_mul_f32_e32 v13, v18, v13
	v_and_b32_e32 v19, 0xffff0000, v24
	v_and_b32_e32 v18, 0xffff0000, v88
	v_pk_mul_f32 v[18:19], v[2:3], v[18:19]
	s_nop 0
	v_add_f32_e32 v19, v21, v19
	v_mul_f32_e32 v22, v18, v19
	v_lshlrev_b32_e32 v18, 16, v89
	v_lshlrev_b32_e32 v19, 16, v25
	v_pk_mul_f32 v[18:19], v[16:17], v[18:19]
	s_nop 0
	v_add_f32_e32 v19, v21, v19
	v_mul_f32_e32 v23, v18, v19
	v_and_b32_e32 v19, 0xffff0000, v25
	v_and_b32_e32 v18, 0xffff0000, v89
	v_pk_mul_f32 v[18:19], v[4:5], v[18:19]
	s_nop 0
	v_add_f32_e32 v19, v21, v19
	v_mul_f32_e32 v18, v18, v19
	v_med3_f32 v19, v13, s81, v149
	v_med3_f32 v21, v22, s81, v149
	v_mov_b32_e32 v13, v101
	v_cvt_pk_fp8_f32 v13, v19, v21
	v_med3_f32 v19, v23, s81, v149
	v_med3_f32 v18, v18, s81, v149
	ds_read_b128 v[22:25], v142
	v_cvt_pk_fp8_f32 v13, v19, v18 op_sel:[0,0,1]
	v_lshlrev_b64 v[18:19], 12, v[124:125]
	v_lshl_add_u64 v[18:19], s[68:69], 0, v[18:19]
	v_lshl_add_u64 v[18:19], v[18:19], 0, s[72:73]
	v_lshl_add_u64 v[18:19], v[18:19], 0, v[98:99]
	global_store_dwordx2 v[18:19], v[12:13], off offset:2048
	v_lshlrev_b32_e32 v12, 16, v82
	s_waitcnt lgkmcnt(0)
	v_lshlrev_b32_e32 v13, 16, v22
	v_pk_mul_f32 v[12:13], v[112:113], v[12:13]
	s_waitcnt vmcnt(7)
	v_mov_b32_e32 v21, v243
	v_add_f32_e32 v13, v21, v13
	v_mul_f32_e32 v18, v12, v13
	v_and_b32_e32 v13, 0xffff0000, v22
	v_and_b32_e32 v12, 0xffff0000, v82
	v_pk_mul_f32 v[12:13], v[6:7], v[12:13]
	v_med3_f32 v18, v18, s81, v149
	v_add_f32_e32 v13, v21, v13
	v_mul_f32_e32 v19, v12, v13
	v_lshlrev_b32_e32 v12, 16, v83
	v_lshlrev_b32_e32 v13, 16, v23
	v_pk_mul_f32 v[12:13], v[14:15], v[12:13]
	v_med3_f32 v19, v19, s81, v149
	v_add_f32_e32 v13, v21, v13
	v_mul_f32_e32 v22, v12, v13
	v_and_b32_e32 v13, 0xffff0000, v23
	v_and_b32_e32 v12, 0xffff0000, v83
	v_pk_mul_f32 v[12:13], v[8:9], v[12:13]
	s_nop 0
	v_add_f32_e32 v13, v21, v13
	v_mul_f32_e32 v13, v12, v13
	v_mov_b32_e32 v12, v101
	v_cvt_pk_fp8_f32 v12, v18, v19
	v_med3_f32 v18, v22, s81, v149
	v_med3_f32 v13, v13, s81, v149
	v_lshlrev_b32_e32 v19, 16, v24
	v_cvt_pk_fp8_f32 v12, v18, v13 op_sel:[0,0,1]
	v_lshlrev_b32_e32 v18, 16, v84
	v_pk_mul_f32 v[18:19], v[10:11], v[18:19]
	s_nop 0
	v_add_f32_e32 v13, v21, v19
	v_mul_f32_e32 v13, v18, v13
	v_and_b32_e32 v19, 0xffff0000, v24
	v_and_b32_e32 v18, 0xffff0000, v84
	v_pk_mul_f32 v[18:19], v[2:3], v[18:19]
	s_nop 0
	v_add_f32_e32 v19, v21, v19
	v_mul_f32_e32 v22, v18, v19
	v_lshlrev_b32_e32 v18, 16, v85
	v_lshlrev_b32_e32 v19, 16, v25
	v_pk_mul_f32 v[18:19], v[16:17], v[18:19]
	s_nop 0
	v_add_f32_e32 v19, v21, v19
	v_mul_f32_e32 v23, v18, v19
	v_and_b32_e32 v19, 0xffff0000, v25
	v_and_b32_e32 v18, 0xffff0000, v85
	v_pk_mul_f32 v[18:19], v[4:5], v[18:19]
	s_nop 0
	v_add_f32_e32 v19, v21, v19
	v_mul_f32_e32 v18, v18, v19
	v_med3_f32 v19, v13, s81, v149
	v_med3_f32 v21, v22, s81, v149
	v_mov_b32_e32 v13, v101
	v_cvt_pk_fp8_f32 v13, v19, v21
	v_med3_f32 v19, v23, s81, v149
	v_med3_f32 v18, v18, s81, v149
	ds_read_b128 v[22:25], v143
	v_cvt_pk_fp8_f32 v13, v19, v18 op_sel:[0,0,1]
	v_lshlrev_b64 v[18:19], 12, v[122:123]
	v_lshl_add_u64 v[18:19], s[68:69], 0, v[18:19]
	v_lshl_add_u64 v[18:19], v[18:19], 0, s[72:73]
	v_lshl_add_u64 v[18:19], v[18:19], 0, v[98:99]
	global_store_dwordx2 v[18:19], v[12:13], off offset:2048
	v_lshlrev_b32_e32 v12, 16, v78
	s_waitcnt lgkmcnt(0)
	v_lshlrev_b32_e32 v13, 16, v22
	v_pk_mul_f32 v[12:13], v[112:113], v[12:13]
	s_waitcnt vmcnt(7)
	v_mov_b32_e32 v21, v244
	v_add_f32_e32 v13, v21, v13
	v_mul_f32_e32 v18, v12, v13
	v_and_b32_e32 v13, 0xffff0000, v22
	v_and_b32_e32 v12, 0xffff0000, v78
	v_pk_mul_f32 v[12:13], v[6:7], v[12:13]
	v_med3_f32 v18, v18, s81, v149
	v_add_f32_e32 v13, v21, v13
	v_mul_f32_e32 v19, v12, v13
	v_lshlrev_b32_e32 v12, 16, v79
	v_lshlrev_b32_e32 v13, 16, v23
	v_pk_mul_f32 v[12:13], v[14:15], v[12:13]
	v_med3_f32 v19, v19, s81, v149
	v_add_f32_e32 v13, v21, v13
	v_mul_f32_e32 v22, v12, v13
	v_and_b32_e32 v13, 0xffff0000, v23
	v_and_b32_e32 v12, 0xffff0000, v79
	v_pk_mul_f32 v[12:13], v[8:9], v[12:13]
	s_nop 0
	v_add_f32_e32 v13, v21, v13
	v_mul_f32_e32 v13, v12, v13
	v_mov_b32_e32 v12, v101
	v_cvt_pk_fp8_f32 v12, v18, v19
	v_med3_f32 v18, v22, s81, v149
	v_med3_f32 v13, v13, s81, v149
	v_lshlrev_b32_e32 v19, 16, v24
	v_cvt_pk_fp8_f32 v12, v18, v13 op_sel:[0,0,1]
	v_lshlrev_b32_e32 v18, 16, v80
	v_pk_mul_f32 v[18:19], v[10:11], v[18:19]
	s_nop 0
	v_add_f32_e32 v13, v21, v19
	v_mul_f32_e32 v13, v18, v13
	v_and_b32_e32 v19, 0xffff0000, v24
	v_and_b32_e32 v18, 0xffff0000, v80
	v_pk_mul_f32 v[18:19], v[2:3], v[18:19]
	s_nop 0
	v_add_f32_e32 v19, v21, v19
	v_mul_f32_e32 v22, v18, v19
	v_lshlrev_b32_e32 v18, 16, v81
	v_lshlrev_b32_e32 v19, 16, v25
	v_pk_mul_f32 v[18:19], v[16:17], v[18:19]
	s_nop 0
	v_add_f32_e32 v19, v21, v19
	v_mul_f32_e32 v23, v18, v19
	v_and_b32_e32 v19, 0xffff0000, v25
	v_and_b32_e32 v18, 0xffff0000, v81
	v_pk_mul_f32 v[18:19], v[4:5], v[18:19]
	s_nop 0
	v_add_f32_e32 v19, v21, v19
	v_mul_f32_e32 v18, v18, v19
	v_med3_f32 v19, v13, s81, v149
	v_med3_f32 v21, v22, s81, v149
	v_mov_b32_e32 v13, v101
	v_cvt_pk_fp8_f32 v13, v19, v21
	v_med3_f32 v19, v23, s81, v149
	v_med3_f32 v18, v18, s81, v149
	ds_read_b128 v[22:25], v144
	v_cvt_pk_fp8_f32 v13, v19, v18 op_sel:[0,0,1]
	v_lshlrev_b64 v[18:19], 12, v[120:121]
	v_lshl_add_u64 v[18:19], s[68:69], 0, v[18:19]
	v_lshl_add_u64 v[18:19], v[18:19], 0, s[72:73]
	v_lshl_add_u64 v[18:19], v[18:19], 0, v[98:99]
	global_store_dwordx2 v[18:19], v[12:13], off offset:2048
	v_lshlrev_b32_e32 v12, 16, v74
	s_waitcnt lgkmcnt(0)
; #define GAS __attribute__((address_space(1)))
; #define LAS __attribute__((address_space(3)))
; __device__ __forceinline__ void sgu_unit(Frame& F, int unit) {
;     ...
; #pragma unroll
;     for (int i = 0; i < 8; ++i) { const v4u fw = *(const LAS v4u*)(L + (rs_ + 16 * i) * 512 + q_ * 16); const float bb = F.sgb[g * GMC + rs_ + 16 * i]; v2u o;
;         o.x = pk4_fp8(S_YB * bflo(uu[i].x) * (bflo(fw.x) * g0.x + bb), S_YB * bfhi(uu[i].x) * (bfhi(fw.x) * g0.y + bb), S_YB * bflo(uu[i].y) * (bflo(fw.y) * g0.z + bb), S_YB * bfhi(uu[i].y) * (bfhi(fw.y) * g0.w + bb));
;         o.y = pk4_fp8(S_YB * bflo(uu[i].z) * (bflo(fw.z) * g1.x + bb), S_YB * bfhi(uu[i].z) * (bfhi(fw.z) * g1.y + bb), S_YB * bflo(uu[i].w) * (bflo(fw.w) * g1.z + bb), S_YB * bfhi(uu[i].w) * (bfhi(fw.w) * g1.w + bb));
;         *(GAS v2u*)((unsigned char*)F.YA + (size_t)(r0 + rs_ + 16 * i) * (2 * ATTW) + ATTW + c0 + 8 * q_) = o; }
	v_lshlrev_b32_e32 v13, 16, v22
	v_pk_mul_f32 v[12:13], v[112:113], v[12:13]
	s_waitcnt vmcnt(7)
	v_mov_b32_e32 v21, v245
	v_add_f32_e32 v13, v21, v13
	v_mul_f32_e32 v18, v12, v13
	v_and_b32_e32 v13, 0xffff0000, v22
	v_and_b32_e32 v12, 0xffff0000, v74
	v_pk_mul_f32 v[12:13], v[6:7], v[12:13]
	v_med3_f32 v18, v18, s81, v149
	v_add_f32_e32 v13, v21, v13
	v_mul_f32_e32 v19, v12, v13
	v_lshlrev_b32_e32 v12, 16, v75
	v_lshlrev_b32_e32 v13, 16, v23
	v_pk_mul_f32 v[12:13], v[14:15], v[12:13]
	v_med3_f32 v19, v19, s81, v149
	v_add_f32_e32 v13, v21, v13
	v_mul_f32_e32 v22, v12, v13
	v_and_b32_e32 v13, 0xffff0000, v23
	v_and_b32_e32 v12, 0xffff0000, v75
	v_pk_mul_f32 v[12:13], v[8:9], v[12:13]
	s_nop 0
	v_add_f32_e32 v13, v21, v13
	v_mul_f32_e32 v13, v12, v13
	v_mov_b32_e32 v12, v101
	v_cvt_pk_fp8_f32 v12, v18, v19
	v_med3_f32 v18, v22, s81, v149
	v_med3_f32 v13, v13, s81, v149
	v_lshlrev_b32_e32 v19, 16, v24
	v_cvt_pk_fp8_f32 v12, v18, v13 op_sel:[0,0,1]
	v_lshlrev_b32_e32 v18, 16, v76
	v_pk_mul_f32 v[18:19], v[10:11], v[18:19]
	s_nop 0
	v_add_f32_e32 v13, v21, v19
	v_mul_f32_e32 v13, v18, v13
	v_and_b32_e32 v19, 0xffff0000, v24
	v_and_b32_e32 v18, 0xffff0000, v76
	v_pk_mul_f32 v[18:19], v[2:3], v[18:19]
	s_nop 0
	v_add_f32_e32 v19, v21, v19
	v_mul_f32_e32 v22, v18, v19
	v_lshlrev_b32_e32 v18, 16, v77
	v_lshlrev_b32_e32 v19, 16, v25
	v_pk_mul_f32 v[18:19], v[16:17], v[18:19]
	s_nop 0
	v_add_f32_e32 v19, v21, v19
	v_mul_f32_e32 v23, v18, v19
	v_and_b32_e32 v19, 0xffff0000, v25
	v_and_b32_e32 v18, 0xffff0000, v77
	v_pk_mul_f32 v[18:19], v[4:5], v[18:19]
	s_nop 0
	v_add_f32_e32 v19, v21, v19
	v_mul_f32_e32 v18, v18, v19
	v_med3_f32 v19, v13, s81, v149
	v_med3_f32 v21, v22, s81, v149
	v_mov_b32_e32 v13, v101
	v_cvt_pk_fp8_f32 v13, v19, v21
	v_med3_f32 v19, v23, s81, v149
	v_med3_f32 v18, v18, s81, v149
	ds_read_b128 v[22:25], v145
	v_cvt_pk_fp8_f32 v13, v19, v18 op_sel:[0,0,1]
	v_lshlrev_b64 v[18:19], 12, v[118:119]
	v_lshl_add_u64 v[18:19], s[68:69], 0, v[18:19]
	v_lshl_add_u64 v[18:19], v[18:19], 0, s[72:73]
	v_lshl_add_u64 v[18:19], v[18:19], 0, v[98:99]
	global_store_dwordx2 v[18:19], v[12:13], off offset:2048
	v_lshlrev_b32_e32 v12, 16, v70
	s_waitcnt lgkmcnt(0)
	v_lshlrev_b32_e32 v13, 16, v22
	v_pk_mul_f32 v[12:13], v[112:113], v[12:13]
	s_waitcnt vmcnt(7)
	v_mov_b32_e32 v21, v246
	v_add_f32_e32 v13, v21, v13
	v_mul_f32_e32 v18, v12, v13
	v_and_b32_e32 v13, 0xffff0000, v22
	v_and_b32_e32 v12, 0xffff0000, v70
	v_pk_mul_f32 v[12:13], v[6:7], v[12:13]
	v_med3_f32 v18, v18, s81, v149
	v_add_f32_e32 v13, v21, v13
	v_mul_f32_e32 v19, v12, v13
	v_lshlrev_b32_e32 v12, 16, v71
	v_lshlrev_b32_e32 v13, 16, v23
	v_pk_mul_f32 v[12:13], v[14:15], v[12:13]
	v_med3_f32 v19, v19, s81, v149
	v_add_f32_e32 v13, v21, v13
	v_mul_f32_e32 v22, v12, v13
	v_and_b32_e32 v13, 0xffff0000, v23
	v_and_b32_e32 v12, 0xffff0000, v71
	v_pk_mul_f32 v[12:13], v[8:9], v[12:13]
	s_nop 0
	v_add_f32_e32 v13, v21, v13
	v_mul_f32_e32 v13, v12, v13
	v_mov_b32_e32 v12, v101
	v_cvt_pk_fp8_f32 v12, v18, v19
	v_med3_f32 v18, v22, s81, v149
	v_med3_f32 v13, v13, s81, v149
	v_lshlrev_b32_e32 v19, 16, v24
	v_cvt_pk_fp8_f32 v12, v18, v13 op_sel:[0,0,1]
	v_lshlrev_b32_e32 v18, 16, v72
	v_pk_mul_f32 v[18:19], v[10:11], v[18:19]
	s_nop 0
	v_add_f32_e32 v13, v21, v19
	v_mul_f32_e32 v13, v18, v13
	v_and_b32_e32 v19, 0xffff0000, v24
	v_and_b32_e32 v18, 0xffff0000, v72
	v_pk_mul_f32 v[18:19], v[2:3], v[18:19]
	s_nop 0
	v_add_f32_e32 v19, v21, v19
	v_mul_f32_e32 v22, v18, v19
	v_lshlrev_b32_e32 v18, 16, v73
	v_lshlrev_b32_e32 v19, 16, v25
	v_pk_mul_f32 v[18:19], v[16:17], v[18:19]
	s_nop 0
	v_add_f32_e32 v19, v21, v19
	v_mul_f32_e32 v23, v18, v19
	v_and_b32_e32 v19, 0xffff0000, v25
	v_and_b32_e32 v18, 0xffff0000, v73
	v_pk_mul_f32 v[18:19], v[4:5], v[18:19]
	s_nop 0
	v_add_f32_e32 v19, v21, v19
	v_mul_f32_e32 v18, v18, v19
	v_med3_f32 v19, v13, s81, v149
	v_med3_f32 v21, v22, s81, v149
	v_mov_b32_e32 v13, v101
	v_cvt_pk_fp8_f32 v13, v19, v21
	v_med3_f32 v19, v23, s81, v149
	v_med3_f32 v18, v18, s81, v149
	ds_read_b128 v[22:25], v146
	v_cvt_pk_fp8_f32 v13, v19, v18 op_sel:[0,0,1]
	v_lshlrev_b64 v[18:19], 12, v[116:117]
	v_lshl_add_u64 v[18:19], s[68:69], 0, v[18:19]
	v_lshl_add_u64 v[18:19], v[18:19], 0, s[72:73]
	v_lshl_add_u64 v[18:19], v[18:19], 0, v[98:99]
	global_store_dwordx2 v[18:19], v[12:13], off offset:2048
	v_lshlrev_b32_e32 v12, 16, v66
	s_waitcnt lgkmcnt(0)
	v_lshlrev_b32_e32 v13, 16, v22
	v_pk_mul_f32 v[12:13], v[112:113], v[12:13]
	s_waitcnt vmcnt(7)
	v_mov_b32_e32 v18, v247
	v_add_f32_e32 v13, v18, v13
	v_mul_f32_e32 v19, v12, v13
	v_and_b32_e32 v13, 0xffff0000, v22
	v_and_b32_e32 v12, 0xffff0000, v66
	v_pk_mul_f32 v[6:7], v[6:7], v[12:13]
	s_nop 0
	v_add_f32_e32 v7, v18, v7
	v_mul_f32_e32 v12, v6, v7
	v_lshlrev_b32_e32 v6, 16, v67
	v_lshlrev_b32_e32 v7, 16, v23
	v_pk_mul_f32 v[6:7], v[14:15], v[6:7]
	s_nop 0
	v_add_f32_e32 v7, v18, v7
	v_mul_f32_e32 v13, v6, v7
	v_and_b32_e32 v7, 0xffff0000, v23
	v_and_b32_e32 v6, 0xffff0000, v67
	v_pk_mul_f32 v[6:7], v[8:9], v[6:7]
	v_med3_f32 v8, v19, s81, v149
	v_add_f32_e32 v7, v18, v7
	v_mul_f32_e32 v7, v6, v7
	v_med3_f32 v9, v12, s81, v149
	v_mov_b32_e32 v6, v101
	v_cvt_pk_fp8_f32 v6, v8, v9
	v_med3_f32 v8, v13, s81, v149
	v_med3_f32 v7, v7, s81, v149
	v_lshlrev_b32_e32 v9, 16, v24
	v_cvt_pk_fp8_f32 v6, v8, v7 op_sel:[0,0,1]
	v_lshlrev_b32_e32 v8, 16, v68
	v_pk_mul_f32 v[8:9], v[10:11], v[8:9]
	s_nop 0
	v_add_f32_e32 v7, v18, v9
	v_mul_f32_e32 v7, v8, v7
	v_and_b32_e32 v9, 0xffff0000, v24
	v_and_b32_e32 v8, 0xffff0000, v68
	v_pk_mul_f32 v[2:3], v[2:3], v[8:9]
	s_nop 0
	v_add_f32_e32 v3, v18, v3
	v_mul_f32_e32 v8, v2, v3
	v_lshlrev_b32_e32 v2, 16, v69
	v_lshlrev_b32_e32 v3, 16, v25
	v_pk_mul_f32 v[2:3], v[16:17], v[2:3]
	s_nop 0
	v_add_f32_e32 v3, v18, v3
	v_mul_f32_e32 v9, v2, v3
	v_and_b32_e32 v3, 0xffff0000, v25
	v_and_b32_e32 v2, 0xffff0000, v69
	v_pk_mul_f32 v[2:3], v[4:5], v[2:3]
	v_med3_f32 v4, v8, s81, v149
	v_add_f32_e32 v3, v18, v3
	v_mul_f32_e32 v2, v2, v3
	v_med3_f32 v3, v7, s81, v149
	v_mov_b32_e32 v7, v101
	v_cvt_pk_fp8_f32 v7, v3, v4
	v_med3_f32 v3, v9, s81, v149
	v_med3_f32 v2, v2, s81, v149
	v_cvt_pk_fp8_f32 v7, v3, v2 op_sel:[0,0,1]
	v_lshlrev_b64 v[2:3], 12, v[114:115]
	v_lshl_add_u64 v[2:3], s[68:69], 0, v[2:3]
	v_lshl_add_u64 v[2:3], v[2:3], 0, s[72:73]
	v_lshl_add_u64 v[2:3], v[2:3], 0, v[98:99]
	global_store_dwordx2 v[2:3], v[6:7], off offset:2048
	s_cbranch_scc0 .LBB0_1330
